# static s_setprio 1 for waves 4-7 during phase 3 (GLA-local + attention loops)
# speedup vs baseline: 1.0009x; 1.0009x over previous
; #define FRESH_TID() do { ap = fresh_args(); ws = ap->ws; unsigned m1_ = ~0u; asm volatile("" : "+s"(m1_)); lane = (int)__builtin_amdgcn_mbcnt_hi(m1_, __builtin_amdgcn_mbcnt_lo(m1_, 0u)); asm volatile("" : "+v"(lane)); wave = wave0; tid = wave0 * 64 + lane; } while (0)
; template <unsigned MASK, bool ONE>
; __global__ void __launch_bounds__(NTHREADS, 2) fwd_kernel(Args a_unused) {
;     ...
;         if (IN(P + 2, 3)) { FRESH_TID();
;             {
;                 const int hw = (vcu >> 5) & 3, dw = tid & 127; float w2[16];
; #pragma unroll
;                 for (int r = 0; r < 16; ++r) w2[r] = (a.w_alpha2 + (size_t)l * 16 * 512)[r * 512 + hw * 128 + dw];
;                 const float bias = (a.b_alpha2 + (size_t)l * 512)[hw * 128 + dw];
;                 for (int u = vcu; u < NB * 4 * 32; u += G) { GlaPre R; gla_local_issue(R, proj, alow, u, tid);
;                     gla_local_unit(lds, R, proj, alow, w2, bias, qdb_, oib_, dstb_, decb_, u, -1, tid, wave, lane); } }
;             FRESH_TID();
;             for (int u = vcu; u < NB * 12 * 16; u += G) { AttnPre R; attn_issue(R, proj, u, tid, wave, lane); attn_unit(lds, R, proj, atto, lse, u, -1, tid, wave, lane); }
.Lsw_start:
	s_cmpk_ge_u32 s78, 0x100
	s_cbranch_scc0 .Lpr3_skip
	s_setprio 1

; __device__ __forceinline__ void xcd_barrier(const XcdBarrier& b) {
;     asm volatile("s_waitcnt vmcnt(0)" ::: "memory");
;     __syncthreads();
;     if (threadIdx.x == 0) {
;         unsigned* bar = b.bar;
;         __builtin_amdgcn_s_waitcnt(0);
;         unsigned nloc = b.st[0], nx = b.st[1];
;         if (nloc == 0u) { xcd_barrier_complete(bar, b.x, nloc, nx); b.st[0] = nloc; b.st[1] = nx; }
.Lsw_done:
	s_setprio 0
	v_readlane_b32 s2, v253, 0
	v_readlane_b32 s3, v253, 1
	s_getreg_b32 s4, hwreg(HW_REG_XCC_ID, 0, 4)
	s_waitcnt vmcnt(0)
	s_barrier
	s_mov_b64 s[0:1], exec
	v_readlane_b32 s6, v253, 5
	v_readlane_b32 s7, v253, 6
	s_and_b64 s[6:7], s[0:1], s[6:7]
	v_readlane_b32 s76, v255, 19
	v_readlane_b32 s78, v255, 21
	v_readlane_b32 s77, v255, 20
	s_mov_b64 exec, s[6:7]
	s_cbranch_execz .LBB0_413
	v_readlane_b32 s5, v254, 47
	s_load_dwordx2 s[2:3], s[2:3], 0xa0
	s_waitcnt vmcnt(0) expcnt(0) lgkmcnt(0)
	v_mov_b32_e32 v0, s5
	ds_read_b32 v2, v0
	v_readlane_b32 s5, v254, 48
	s_and_b32 s50, s4, 15
	s_waitcnt lgkmcnt(0)
	v_cmp_ne_u32_e32 vcc, 0, v2
	v_mov_b32_e32 v0, s5
	ds_read_b32 v0, v0
	s_cbranch_vccnz .LBB0_377
	v_readlane_b32 s4, v253, 2
	v_readlane_b32 s5, v253, 3
	s_load_dwordx2 s[8:9], s[4:5], 0x4
	s_add_u32 s4, s2, 0x4200
	s_addc_u32 s5, s3, 0
	s_add_u32 s6, s2, 0x4400
	s_addc_u32 s7, s3, 0
	s_waitcnt lgkmcnt(0)
	s_mul_i32 s51, s8, s74
	s_add_u32 s8, s2, 0x4500
	s_mul_i32 s51, s51, s9
	s_addc_u32 s9, s3, 0
	s_add_u32 s10, s2, 0x4600
	s_addc_u32 s11, s3, 0
	s_add_u32 s12, s2, 0x4700
	s_addc_u32 s13, s3, 0
	s_add_u32 s14, s2, 0x4800
	s_addc_u32 s15, s3, 0
	s_add_u32 s16, s2, 0x4900
	s_addc_u32 s17, s3, 0
	s_add_u32 s18, s2, 0x4a00
	s_addc_u32 s19, s3, 0
	s_add_u32 s20, s2, 0x4b00
	s_addc_u32 s21, s3, 0
	s_add_u32 s22, s2, 0x4c00
	s_addc_u32 s23, s3, 0
	s_add_u32 s24, s2, 0x4d00
	s_addc_u32 s25, s3, 0
	s_add_u32 s26, s2, 0x4e00
	s_addc_u32 s27, s3, 0
	s_add_u32 s28, s2, 0x4f00
	s_addc_u32 s29, s3, 0
	s_add_u32 s30, s2, 0x5000
	s_addc_u32 s31, s3, 0
	s_add_u32 s34, s2, 0x5100
	s_addc_u32 s35, s3, 0
	s_add_u32 s36, s2, 0x5200
	s_addc_u32 s37, s3, 0
	s_add_u32 s40, s2, 0x5300
	s_addc_u32 s41, s3, 0
	s_mov_b32 s52, 1
	s_branch .LBB0_365
